# barrier: dropped unused per-XCD generation add, leader invalidate issued with the top arrival atomic
# baseline (speedup 1.0000x reference)
; __device__ __forceinline__ unsigned xb_ld(unsigned* p)              { return __hip_atomic_load(p, __ATOMIC_RELAXED, __HIP_MEMORY_SCOPE_AGENT); }
; __device__ __forceinline__ unsigned xb_add(unsigned* p, unsigned v) { return __hip_atomic_fetch_add(p, v, __ATOMIC_RELAXED, __HIP_MEMORY_SCOPE_AGENT); }
; #define XB_SPIN(cond, bar) do { unsigned _sp = 0; while (cond) { __builtin_amdgcn_s_sleep(1); \
;     if ((++_sp & 255u) == 0u) { if (xb_ld(&(bar)[XB_TMO])) break; if (_sp > XB_SPIN_CAP) { atomicAdd(&(bar)[XB_TMO], 1u); break; } } } } while (0)
; __device__ __forceinline__ void xcd_barrier(const XcdBarrier& b) {
;     ...
;             const unsigned og = xb_add(&bar[XB_TOP], 1u);
;             const unsigned tg = og / nx;
;             if (og + 1u == (tg + 1u) * nx) xb_add(&bar[XB_TOPGEN], 1u);
;             else XB_SPIN(xb_ld(&bar[XB_TOPGEN]) == tg, bar);
;             __builtin_amdgcn_fence(__ATOMIC_ACQUIRE, "agent");
.LBB0_261:
	s_or_b64 exec, exec, s[12:13]
	v_cvt_f32_u32_e32 v3, v0
	buffer_inv sc1
	s_waitcnt vmcnt(0)
	v_readfirstlane_b32 s10, v2
	s_add_u32 s12, s0, 0x7500
	s_addc_u32 s13, s1, 0
	v_rcp_iflag_f32_e32 v3, v3
	v_add_u32_e32 v1, s10, v1
	v_add_u32_e32 v4, 1, v1
	s_mov_b64 s[14:15], -1
	v_mul_f32_e32 v2, 0x4f7ffffe, v3
	v_cvt_u32_f32_e32 v2, v2
	v_sub_u32_e32 v3, 0, v0
	v_mul_lo_u32 v3, v3, v2
	v_mul_hi_u32 v3, v2, v3
	v_add_u32_e32 v2, v2, v3
	v_mul_hi_u32 v2, v1, v2
	v_mul_lo_u32 v3, v2, v0
	v_sub_u32_e32 v1, v1, v3
	v_add_u32_e32 v5, 1, v2
	v_cmp_ge_u32_e32 vcc, v1, v0
	v_sub_u32_e32 v3, v1, v0
	s_nop 0
	v_cndmask_b32_e32 v2, v2, v5, vcc
	v_cndmask_b32_e32 v1, v1, v3, vcc
	v_add_u32_e32 v3, 1, v2
	v_cmp_ge_u32_e32 vcc, v1, v0
	s_nop 1
	v_cndmask_b32_e32 v2, v2, v3, vcc
	v_mul_lo_u32 v1, v0, v2
	v_add_u32_e32 v0, v1, v0
	v_cmp_ne_u32_e32 vcc, v4, v0
	v_mov_b32_e32 v5, v0
	v_mov_b64_e32 v[0:1], s[12:13]
	s_and_saveexec_b64 s[10:11], vcc
	s_cbranch_execz .LBB0_273
	v_mov_b32_e32 v0, 0
	global_load_dword v1, v0, s[12:13] offset:-256 sc1
	s_mov_b64 s[18:19], 0
	s_waitcnt vmcnt(0)
	v_cmp_gt_u32_e32 vcc, v5, v1
	s_and_saveexec_b64 s[16:17], vcc
	s_cbranch_execz .LBB0_272
	s_add_u32 s14, s0, 0x4200
	s_addc_u32 s15, s1, 0
	s_mov_b32 s28, 1
	s_branch .LBB0_265

; __device__ __forceinline__ unsigned xb_add(unsigned* p, unsigned v) { return __hip_atomic_fetch_add(p, v, __ATOMIC_RELAXED, __HIP_MEMORY_SCOPE_AGENT); }
; __device__ __forceinline__ void xcd_barrier(const XcdBarrier& b) {
;     ...
;             __builtin_amdgcn_fence(__ATOMIC_ACQUIRE, "agent");
;             xb_add(&bar[XB_XGEN(b.x)], 1u);
;             asm volatile("s_waitcnt vmcnt(0)" ::: "memory");
.LBB0_275:
	s_or_b64 exec, exec, s[10:11]
	s_mov_b64 s[10:11], exec
	v_mbcnt_lo_u32_b32 v0, s10, 0
	v_mbcnt_hi_u32_b32 v0, s11, v0
	v_cmp_eq_u32_e32 vcc, 0, v0
	s_waitcnt vmcnt(0)
	s_and_saveexec_b64 s[12:13], vcc
	s_cbranch_execz .LBB0_277
	s_bcnt1_i32_b64 s10, s[10:11]
	v_mov_b32_e32 v0, 0x2000
	v_mov_b32_e32 v1, s10
.LBB0_277:
	s_or_b64 exec, exec, s[12:13]
	s_waitcnt vmcnt(0)

; __device__ __forceinline__ unsigned xb_ld(unsigned* p)              { return __hip_atomic_load(p, __ATOMIC_RELAXED, __HIP_MEMORY_SCOPE_AGENT); }
; __device__ __forceinline__ unsigned xb_add(unsigned* p, unsigned v) { return __hip_atomic_fetch_add(p, v, __ATOMIC_RELAXED, __HIP_MEMORY_SCOPE_AGENT); }
; #define XB_SPIN(cond, bar) do { unsigned _sp = 0; while (cond) { __builtin_amdgcn_s_sleep(1); \
;     if ((++_sp & 255u) == 0u) { if (xb_ld(&(bar)[XB_TMO])) break; if (_sp > XB_SPIN_CAP) { atomicAdd(&(bar)[XB_TMO], 1u); break; } } } } while (0)
; __device__ __forceinline__ void xcd_barrier(const XcdBarrier& b) {
;     ...
;             const unsigned og = xb_add(&bar[XB_TOP], 1u);
;             const unsigned tg = og / nx;
;             if (og + 1u == (tg + 1u) * nx) xb_add(&bar[XB_TOPGEN], 1u);
;             else XB_SPIN(xb_ld(&bar[XB_TOPGEN]) == tg, bar);
;             __builtin_amdgcn_fence(__ATOMIC_ACQUIRE, "agent");
.LBB0_487:
	s_or_b64 exec, exec, s[38:39]
	buffer_inv sc1
	s_waitcnt vmcnt(0)
	v_readfirstlane_b32 s7, v3
	v_sub_u32_e32 v4, 0, v2
	v_readlane_b32 s8, v252, 8
	v_add_u32_e32 v3, s7, v0
	v_cvt_f32_u32_e32 v0, v2
	v_readlane_b32 s9, v252, 9
	s_mov_b64 s[38:39], -1
	v_rcp_iflag_f32_e32 v0, v0
	s_nop 0
	v_mul_f32_e32 v0, 0x4f7ffffe, v0
	v_cvt_u32_f32_e32 v0, v0
	v_mul_lo_u32 v4, v4, v0
	v_mul_hi_u32 v4, v0, v4
	v_add_u32_e32 v0, v0, v4
	v_mul_hi_u32 v0, v3, v0
	v_mul_lo_u32 v4, v0, v2
	v_sub_u32_e32 v4, v3, v4
	v_cmp_ge_u32_e32 vcc, v4, v2
	v_add_u32_e32 v5, 1, v0
	v_add_u32_e32 v3, 1, v3
	v_cndmask_b32_e32 v0, v0, v5, vcc
	v_sub_u32_e32 v5, v4, v2
	v_cndmask_b32_e32 v4, v4, v5, vcc
	v_cmp_ge_u32_e32 vcc, v4, v2
	v_add_u32_e32 v4, 1, v0
	s_nop 0
	v_cndmask_b32_e32 v0, v0, v4, vcc
	v_mul_lo_u32 v4, v2, v0
	v_add_u32_e32 v2, v4, v2
	v_cmp_ne_u32_e32 vcc, v3, v2
	v_mov_b32_e32 v5, v2
	v_mov_b64_e32 v[2:3], s[8:9]
	s_and_saveexec_b64 s[36:37], vcc
	s_cbranch_execz .LBB0_499
	v_readlane_b32 s8, v252, 6
	v_readlane_b32 s9, v252, 7
	s_mov_b64 s[40:41], 0
	s_nop 3
	global_load_dword v2, v1, s[8:9] sc1
	s_waitcnt vmcnt(0)
	v_cmp_gt_u32_e32 vcc, v5, v2
	s_and_saveexec_b64 s[38:39], vcc
	s_cbranch_execz .LBB0_498
	s_mov_b32 s7, 1
	s_branch .LBB0_491

; __device__ __forceinline__ unsigned xb_add(unsigned* p, unsigned v) { return __hip_atomic_fetch_add(p, v, __ATOMIC_RELAXED, __HIP_MEMORY_SCOPE_AGENT); }
; __device__ __forceinline__ void xcd_barrier(const XcdBarrier& b) {
;     ...
;             __builtin_amdgcn_fence(__ATOMIC_ACQUIRE, "agent");
;             xb_add(&bar[XB_XGEN(b.x)], 1u);
;             asm volatile("s_waitcnt vmcnt(0)" ::: "memory");
.LBB0_501:
	s_or_b64 exec, exec, s[36:37]
	s_mov_b64 s[36:37], exec
	v_mbcnt_lo_u32_b32 v0, s36, 0
	v_mbcnt_hi_u32_b32 v0, s37, v0
	v_cmp_eq_u32_e32 vcc, 0, v0
	s_waitcnt vmcnt(0)
	s_and_saveexec_b64 s[38:39], vcc
	s_cbranch_execz .LBB0_503
	s_bcnt1_i32_b64 s7, s[36:37]
	v_readlane_b32 s8, v252, 4
	v_mov_b32_e32 v0, s7
	v_readlane_b32 s9, v252, 5
	s_nop 4
.LBB0_503:
	s_or_b64 exec, exec, s[38:39]
	s_waitcnt vmcnt(0)

; __device__ __forceinline__ unsigned xb_add(unsigned* p, unsigned v) { return __hip_atomic_fetch_add(p, v, __ATOMIC_RELAXED, __HIP_MEMORY_SCOPE_AGENT); }
; __device__ __forceinline__ void xcd_barrier(const XcdBarrier& b) {
;     ...
;             __builtin_amdgcn_fence(__ATOMIC_ACQUIRE, "agent");
;             xb_add(&bar[XB_XGEN(b.x)], 1u);
;             asm volatile("s_waitcnt vmcnt(0)" ::: "memory");
.LBB0_631:
	s_or_b64 exec, exec, s[36:37]
	s_mov_b64 s[36:37], exec
	v_mbcnt_lo_u32_b32 v0, s36, 0
	v_mbcnt_hi_u32_b32 v0, s37, v0
	v_cmp_eq_u32_e32 vcc, 0, v0
	s_waitcnt vmcnt(0)
	s_and_saveexec_b64 s[38:39], vcc
	s_cbranch_execz .LBB0_633
	s_bcnt1_i32_b64 s7, s[36:37]
	v_readlane_b32 s8, v252, 4
	v_mov_b32_e32 v0, s7
	v_readlane_b32 s9, v252, 5
	s_nop 4
.LBB0_633:
	s_or_b64 exec, exec, s[38:39]
	s_waitcnt vmcnt(0)

; __device__ __forceinline__ unsigned xb_ld(unsigned* p)              { return __hip_atomic_load(p, __ATOMIC_RELAXED, __HIP_MEMORY_SCOPE_AGENT); }
; __device__ __forceinline__ unsigned xb_add(unsigned* p, unsigned v) { return __hip_atomic_fetch_add(p, v, __ATOMIC_RELAXED, __HIP_MEMORY_SCOPE_AGENT); }
; #define XB_SPIN(cond, bar) do { unsigned _sp = 0; while (cond) { __builtin_amdgcn_s_sleep(1); \
;     if ((++_sp & 255u) == 0u) { if (xb_ld(&(bar)[XB_TMO])) break; if (_sp > XB_SPIN_CAP) { atomicAdd(&(bar)[XB_TMO], 1u); break; } } } } while (0)
; __device__ __forceinline__ void xcd_barrier(const XcdBarrier& b) {
;     ...
;             const unsigned og = xb_add(&bar[XB_TOP], 1u);
;             const unsigned tg = og / nx;
;             if (og + 1u == (tg + 1u) * nx) xb_add(&bar[XB_TOPGEN], 1u);
;             else XB_SPIN(xb_ld(&bar[XB_TOPGEN]) == tg, bar);
;             __builtin_amdgcn_fence(__ATOMIC_ACQUIRE, "agent");
.LBB0_753:
	s_or_b64 exec, exec, s[38:39]
	buffer_inv sc1
	s_waitcnt vmcnt(0)
	v_readfirstlane_b32 s6, v3
	v_sub_u32_e32 v4, 0, v2
	s_mov_b64 s[38:39], -1
	v_add_u32_e32 v3, s6, v0
	v_cvt_f32_u32_e32 v0, v2
	v_readlane_b32 s6, v252, 8
	v_readlane_b32 s7, v252, 9
	v_rcp_iflag_f32_e32 v0, v0
	s_nop 0
	v_mul_f32_e32 v0, 0x4f7ffffe, v0
	v_cvt_u32_f32_e32 v0, v0
	v_mul_lo_u32 v4, v4, v0
	v_mul_hi_u32 v4, v0, v4
	v_add_u32_e32 v0, v0, v4
	v_mul_hi_u32 v0, v3, v0
	v_mul_lo_u32 v4, v0, v2
	v_sub_u32_e32 v4, v3, v4
	v_cmp_ge_u32_e32 vcc, v4, v2
	v_add_u32_e32 v5, 1, v0
	v_add_u32_e32 v3, 1, v3
	v_cndmask_b32_e32 v0, v0, v5, vcc
	v_sub_u32_e32 v5, v4, v2
	v_cndmask_b32_e32 v4, v4, v5, vcc
	v_cmp_ge_u32_e32 vcc, v4, v2
	v_add_u32_e32 v4, 1, v0
	s_nop 0
	v_cndmask_b32_e32 v0, v0, v4, vcc
	v_mul_lo_u32 v4, v2, v0
	v_add_u32_e32 v2, v4, v2
	v_cmp_ne_u32_e32 vcc, v3, v2
	v_mov_b32_e32 v5, v2
	v_mov_b64_e32 v[2:3], s[6:7]
	s_and_saveexec_b64 s[36:37], vcc
	s_cbranch_execz .LBB0_765
	v_readlane_b32 s6, v252, 6
	v_readlane_b32 s7, v252, 7
	s_mov_b64 s[40:41], 0
	s_nop 3
	global_load_dword v2, v1, s[6:7] sc1
	s_waitcnt vmcnt(0)
	v_cmp_gt_u32_e32 vcc, v5, v2
	s_and_saveexec_b64 s[38:39], vcc
	s_cbranch_execz .LBB0_764
	s_mov_b32 s6, 1
	s_branch .LBB0_757

; __device__ __forceinline__ unsigned xb_add(unsigned* p, unsigned v) { return __hip_atomic_fetch_add(p, v, __ATOMIC_RELAXED, __HIP_MEMORY_SCOPE_AGENT); }
; __device__ __forceinline__ void xcd_barrier(const XcdBarrier& b) {
;     ...
;             __builtin_amdgcn_fence(__ATOMIC_ACQUIRE, "agent");
;             xb_add(&bar[XB_XGEN(b.x)], 1u);
;             asm volatile("s_waitcnt vmcnt(0)" ::: "memory");
.LBB0_767:
	s_or_b64 exec, exec, s[36:37]
	s_mov_b64 s[36:37], exec
	v_mbcnt_lo_u32_b32 v0, s36, 0
	v_mbcnt_hi_u32_b32 v0, s37, v0
	v_cmp_eq_u32_e32 vcc, 0, v0
	s_waitcnt vmcnt(0)
	s_and_saveexec_b64 s[38:39], vcc
	s_cbranch_execz .LBB0_769
	s_bcnt1_i32_b64 s6, s[36:37]
	v_mov_b32_e32 v0, s6
	v_readlane_b32 s6, v252, 4
	v_readlane_b32 s7, v252, 5
	s_nop 4
.LBB0_769:
	s_or_b64 exec, exec, s[38:39]
	s_waitcnt vmcnt(0)

; __device__ __forceinline__ unsigned xb_add(unsigned* p, unsigned v) { return __hip_atomic_fetch_add(p, v, __ATOMIC_RELAXED, __HIP_MEMORY_SCOPE_AGENT); }
; __device__ __forceinline__ void xcd_barrier(const XcdBarrier& b) {
;     ...
;             __builtin_amdgcn_fence(__ATOMIC_ACQUIRE, "agent");
;             xb_add(&bar[XB_XGEN(b.x)], 1u);
;             asm volatile("s_waitcnt vmcnt(0)" ::: "memory");
.LBB0_1054:
	s_or_b64 exec, exec, s[36:37]
	s_mov_b64 s[36:37], exec
	v_mbcnt_lo_u32_b32 v0, s36, 0
	v_mbcnt_hi_u32_b32 v0, s37, v0
	v_cmp_eq_u32_e32 vcc, 0, v0
	s_waitcnt vmcnt(0)
	s_and_saveexec_b64 s[38:39], vcc
	s_cbranch_execz .LBB0_1056
	s_bcnt1_i32_b64 s7, s[36:37]
	v_readlane_b32 s8, v252, 4
	v_mov_b32_e32 v0, s7
	v_readlane_b32 s9, v252, 5
	s_nop 4
.LBB0_1056:
	s_or_b64 exec, exec, s[38:39]
	s_waitcnt vmcnt(0)

; __device__ __forceinline__ unsigned xb_add(unsigned* p, unsigned v) { return __hip_atomic_fetch_add(p, v, __ATOMIC_RELAXED, __HIP_MEMORY_SCOPE_AGENT); }
; __device__ __forceinline__ void xcd_barrier(const XcdBarrier& b) {
;     ...
;             __builtin_amdgcn_fence(__ATOMIC_ACQUIRE, "agent");
;             xb_add(&bar[XB_XGEN(b.x)], 1u);
;             asm volatile("s_waitcnt vmcnt(0)" ::: "memory");
.LBB0_1174:
	s_or_b64 exec, exec, s[36:37]
	s_mov_b64 s[36:37], exec
	v_mbcnt_lo_u32_b32 v0, s36, 0
	v_mbcnt_hi_u32_b32 v0, s37, v0
	v_cmp_eq_u32_e32 vcc, 0, v0
	s_waitcnt vmcnt(0)
	s_and_saveexec_b64 s[38:39], vcc
	s_cbranch_execz .LBB0_1176
	s_bcnt1_i32_b64 s7, s[36:37]
	v_readlane_b32 s8, v252, 4
	v_mov_b32_e32 v0, s7
	v_readlane_b32 s9, v252, 5
	s_nop 4
.LBB0_1176:
	s_or_b64 exec, exec, s[38:39]
	s_waitcnt vmcnt(0)

; __device__ __forceinline__ unsigned xb_add(unsigned* p, unsigned v) { return __hip_atomic_fetch_add(p, v, __ATOMIC_RELAXED, __HIP_MEMORY_SCOPE_AGENT); }
; __device__ __forceinline__ void xcd_barrier(const XcdBarrier& b) {
;     ...
;             __builtin_amdgcn_fence(__ATOMIC_ACQUIRE, "agent");
;             xb_add(&bar[XB_XGEN(b.x)], 1u);
;             asm volatile("s_waitcnt vmcnt(0)" ::: "memory");
.LBB0_1261:
	s_or_b64 exec, exec, s[36:37]
	s_mov_b64 s[36:37], exec
	v_mbcnt_lo_u32_b32 v0, s36, 0
	v_mbcnt_hi_u32_b32 v0, s37, v0
	v_cmp_eq_u32_e32 vcc, 0, v0
	s_waitcnt vmcnt(0)
	s_and_saveexec_b64 s[38:39], vcc
	s_cbranch_execz .LBB0_1263
	s_bcnt1_i32_b64 s7, s[36:37]
	v_readlane_b32 s8, v252, 4
	v_mov_b32_e32 v0, s7
	v_readlane_b32 s9, v252, 5
	s_nop 4
.LBB0_1263:
	s_or_b64 exec, exec, s[38:39]
	s_waitcnt vmcnt(0)

; __device__ __forceinline__ unsigned xb_ld(unsigned* p)              { return __hip_atomic_load(p, __ATOMIC_RELAXED, __HIP_MEMORY_SCOPE_AGENT); }
; __device__ __forceinline__ unsigned xb_add(unsigned* p, unsigned v) { return __hip_atomic_fetch_add(p, v, __ATOMIC_RELAXED, __HIP_MEMORY_SCOPE_AGENT); }
; #define XB_SPIN(cond, bar) do { unsigned _sp = 0; while (cond) { __builtin_amdgcn_s_sleep(1); \
;     if ((++_sp & 255u) == 0u) { if (xb_ld(&(bar)[XB_TMO])) break; if (_sp > XB_SPIN_CAP) { atomicAdd(&(bar)[XB_TMO], 1u); break; } } } } while (0)
; __device__ __forceinline__ void xcd_barrier(const XcdBarrier& b) {
;     ...
;             const unsigned og = xb_add(&bar[XB_TOP], 1u);
;             const unsigned tg = og / nx;
;             if (og + 1u == (tg + 1u) * nx) xb_add(&bar[XB_TOPGEN], 1u);
;             else XB_SPIN(xb_ld(&bar[XB_TOPGEN]) == tg, bar);
;             __builtin_amdgcn_fence(__ATOMIC_ACQUIRE, "agent");
.LBB0_1358:
	s_or_b64 exec, exec, s[40:41]
	buffer_inv sc1
	s_waitcnt vmcnt(0)
	v_readfirstlane_b32 s7, v3
	v_sub_u32_e32 v4, 0, v2
	v_readlane_b32 s8, v252, 8
	v_add_u32_e32 v3, s7, v0
	v_cvt_f32_u32_e32 v0, v2
	v_readlane_b32 s9, v252, 9
	s_mov_b64 s[40:41], -1
	v_rcp_iflag_f32_e32 v0, v0
	s_nop 0
	v_mul_f32_e32 v0, 0x4f7ffffe, v0
	v_cvt_u32_f32_e32 v0, v0
	v_mul_lo_u32 v4, v4, v0
	v_mul_hi_u32 v4, v0, v4
	v_add_u32_e32 v0, v0, v4
	v_mul_hi_u32 v0, v3, v0
	v_mul_lo_u32 v4, v0, v2
	v_sub_u32_e32 v4, v3, v4
	v_cmp_ge_u32_e32 vcc, v4, v2
	v_add_u32_e32 v5, 1, v0
	v_add_u32_e32 v3, 1, v3
	v_cndmask_b32_e32 v0, v0, v5, vcc
	v_sub_u32_e32 v5, v4, v2
	v_cndmask_b32_e32 v4, v4, v5, vcc
	v_cmp_ge_u32_e32 vcc, v4, v2
	v_add_u32_e32 v4, 1, v0
	s_nop 0
	v_cndmask_b32_e32 v0, v0, v4, vcc
	v_mul_lo_u32 v4, v2, v0
	v_add_u32_e32 v2, v4, v2
	v_cmp_ne_u32_e32 vcc, v3, v2
	v_mov_b32_e32 v5, v2
	v_mov_b64_e32 v[2:3], s[8:9]
	s_and_saveexec_b64 s[38:39], vcc
	s_cbranch_execz .LBB0_1370
	v_readlane_b32 s8, v252, 6
	v_readlane_b32 s9, v252, 7
	s_mov_b64 s[44:45], 0
	s_nop 3
	global_load_dword v2, v1, s[8:9] sc1
	s_waitcnt vmcnt(0)
	v_cmp_gt_u32_e32 vcc, v5, v2
	s_and_saveexec_b64 s[40:41], vcc
	s_cbranch_execz .LBB0_1369
	s_mov_b32 s7, 1
	s_branch .LBB0_1362

; __device__ __forceinline__ unsigned xb_ld(unsigned* p)              { return __hip_atomic_load(p, __ATOMIC_RELAXED, __HIP_MEMORY_SCOPE_AGENT); }
; __device__ __forceinline__ unsigned xb_add(unsigned* p, unsigned v) { return __hip_atomic_fetch_add(p, v, __ATOMIC_RELAXED, __HIP_MEMORY_SCOPE_AGENT); }
; #define XB_SPIN(cond, bar) do { unsigned _sp = 0; while (cond) { __builtin_amdgcn_s_sleep(1); \
;     if ((++_sp & 255u) == 0u) { if (xb_ld(&(bar)[XB_TMO])) break; if (_sp > XB_SPIN_CAP) { atomicAdd(&(bar)[XB_TMO], 1u); break; } } } } while (0)
; __device__ __forceinline__ void xcd_barrier(const XcdBarrier& b) {
;     ...
;             const unsigned og = xb_add(&bar[XB_TOP], 1u);
;             const unsigned tg = og / nx;
;             if (og + 1u == (tg + 1u) * nx) xb_add(&bar[XB_TOPGEN], 1u);
;             else XB_SPIN(xb_ld(&bar[XB_TOPGEN]) == tg, bar);
;             __builtin_amdgcn_fence(__ATOMIC_ACQUIRE, "agent");
;             xb_add(&bar[XB_XGEN(b.x)], 1u);
;             asm volatile("s_waitcnt vmcnt(0)" ::: "memory");
.LBB0_1372:
	s_or_b64 exec, exec, s[38:39]
	s_mov_b64 s[38:39], exec
	v_mbcnt_lo_u32_b32 v0, s38, 0
	v_mbcnt_hi_u32_b32 v0, s39, v0
	v_cmp_eq_u32_e32 vcc, 0, v0
	s_waitcnt vmcnt(0)
	s_and_saveexec_b64 s[40:41], vcc
	s_cbranch_execz .LBB0_1374
	s_bcnt1_i32_b64 s7, s[38:39]
	v_readlane_b32 s8, v252, 4
	v_mov_b32_e32 v0, s7
	v_readlane_b32 s9, v252, 5
	s_nop 4
.LBB0_1374:
	s_or_b64 exec, exec, s[40:41]
	s_waitcnt vmcnt(0)

; __device__ __forceinline__ unsigned xb_ld(unsigned* p)              { return __hip_atomic_load(p, __ATOMIC_RELAXED, __HIP_MEMORY_SCOPE_AGENT); }
; __device__ __forceinline__ unsigned xb_add(unsigned* p, unsigned v) { return __hip_atomic_fetch_add(p, v, __ATOMIC_RELAXED, __HIP_MEMORY_SCOPE_AGENT); }
; #define XB_SPIN(cond, bar) do { unsigned _sp = 0; while (cond) { __builtin_amdgcn_s_sleep(1); \
;     if ((++_sp & 255u) == 0u) { if (xb_ld(&(bar)[XB_TMO])) break; if (_sp > XB_SPIN_CAP) { atomicAdd(&(bar)[XB_TMO], 1u); break; } } } } while (0)
; __device__ __forceinline__ void xcd_barrier(const XcdBarrier& b) {
;     ...
;             const unsigned og = xb_add(&bar[XB_TOP], 1u);
;             const unsigned tg = og / nx;
;             if (og + 1u == (tg + 1u) * nx) xb_add(&bar[XB_TOPGEN], 1u);
;             else XB_SPIN(xb_ld(&bar[XB_TOPGEN]) == tg, bar);
;             __builtin_amdgcn_fence(__ATOMIC_ACQUIRE, "agent");
;             xb_add(&bar[XB_XGEN(b.x)], 1u);
;             asm volatile("s_waitcnt vmcnt(0)" ::: "memory");
.LBB0_1449:
	s_or_b64 exec, exec, s[36:37]
	s_mov_b64 s[36:37], exec
	v_mbcnt_lo_u32_b32 v0, s36, 0
	v_mbcnt_hi_u32_b32 v0, s37, v0
	v_cmp_eq_u32_e32 vcc, 0, v0
	s_waitcnt vmcnt(0)
	s_and_saveexec_b64 s[38:39], vcc
	s_cbranch_execz .LBB0_1451
	s_bcnt1_i32_b64 s7, s[36:37]
	v_readlane_b32 s8, v252, 4
	v_mov_b32_e32 v0, s7
	v_readlane_b32 s9, v252, 5
	s_nop 4
.LBB0_1451:
	s_or_b64 exec, exec, s[38:39]
	s_waitcnt vmcnt(0)

; __device__ __forceinline__ unsigned xb_ld(unsigned* p)              { return __hip_atomic_load(p, __ATOMIC_RELAXED, __HIP_MEMORY_SCOPE_AGENT); }
; __device__ __forceinline__ unsigned xb_add(unsigned* p, unsigned v) { return __hip_atomic_fetch_add(p, v, __ATOMIC_RELAXED, __HIP_MEMORY_SCOPE_AGENT); }
; #define XB_SPIN(cond, bar) do { unsigned _sp = 0; while (cond) { __builtin_amdgcn_s_sleep(1); \
;     if ((++_sp & 255u) == 0u) { if (xb_ld(&(bar)[XB_TMO])) break; if (_sp > XB_SPIN_CAP) { atomicAdd(&(bar)[XB_TMO], 1u); break; } } } } while (0)
; __device__ __forceinline__ void xcd_barrier(const XcdBarrier& b) {
;     ...
;             const unsigned og = xb_add(&bar[XB_TOP], 1u);
;             const unsigned tg = og / nx;
;             if (og + 1u == (tg + 1u) * nx) xb_add(&bar[XB_TOPGEN], 1u);
;             else XB_SPIN(xb_ld(&bar[XB_TOPGEN]) == tg, bar);
;             __builtin_amdgcn_fence(__ATOMIC_ACQUIRE, "agent");
;             xb_add(&bar[XB_XGEN(b.x)], 1u);
;             asm volatile("s_waitcnt vmcnt(0)" ::: "memory");
.LBB0_1544:
	s_or_b64 exec, exec, s[36:37]
	s_mov_b64 s[36:37], exec
	v_mbcnt_lo_u32_b32 v0, s36, 0
	v_mbcnt_hi_u32_b32 v0, s37, v0
	v_cmp_eq_u32_e32 vcc, 0, v0
	s_waitcnt vmcnt(0)
	s_and_saveexec_b64 s[38:39], vcc
	s_cbranch_execz .LBB0_1546
	s_bcnt1_i32_b64 s6, s[36:37]
	v_mov_b32_e32 v0, s6
	v_readlane_b32 s6, v252, 4
	v_readlane_b32 s7, v252, 5
	s_nop 4
.LBB0_1546:
	s_or_b64 exec, exec, s[38:39]
	s_waitcnt vmcnt(0)

; __device__ __forceinline__ unsigned xb_ld(unsigned* p)              { return __hip_atomic_load(p, __ATOMIC_RELAXED, __HIP_MEMORY_SCOPE_AGENT); }
; __device__ __forceinline__ unsigned xb_add(unsigned* p, unsigned v) { return __hip_atomic_fetch_add(p, v, __ATOMIC_RELAXED, __HIP_MEMORY_SCOPE_AGENT); }
; #define XB_SPIN(cond, bar) do { unsigned _sp = 0; while (cond) { __builtin_amdgcn_s_sleep(1); \
;     if ((++_sp & 255u) == 0u) { if (xb_ld(&(bar)[XB_TMO])) break; if (_sp > XB_SPIN_CAP) { atomicAdd(&(bar)[XB_TMO], 1u); break; } } } } while (0)
; __device__ __forceinline__ void xcd_barrier(const XcdBarrier& b) {
;     ...
;             const unsigned og = xb_add(&bar[XB_TOP], 1u);
;             const unsigned tg = og / nx;
;             if (og + 1u == (tg + 1u) * nx) xb_add(&bar[XB_TOPGEN], 1u);
;             else XB_SPIN(xb_ld(&bar[XB_TOPGEN]) == tg, bar);
;             __builtin_amdgcn_fence(__ATOMIC_ACQUIRE, "agent");
;             xb_add(&bar[XB_XGEN(b.x)], 1u);
;             asm volatile("s_waitcnt vmcnt(0)" ::: "memory");
.LBB0_1692:
	s_or_b64 exec, exec, s[36:37]
	s_mov_b64 s[36:37], exec
	v_mbcnt_lo_u32_b32 v0, s36, 0
	v_mbcnt_hi_u32_b32 v0, s37, v0
	v_cmp_eq_u32_e32 vcc, 0, v0
	s_waitcnt vmcnt(0)
	s_and_saveexec_b64 s[38:39], vcc
	s_cbranch_execz .LBB0_1549
	s_bcnt1_i32_b64 s6, s[36:37]
	v_mov_b32_e32 v0, s6
	v_readlane_b32 s6, v252, 4
	v_readlane_b32 s7, v252, 5
	s_nop 4
	s_branch .LBB0_1549
